# attention: the static priority raise moved to the other wave half (waves 0-3 instead of 4-7)
# speedup vs baseline: 1.0042x; 1.0022x over previous
.LBB0_487:
	s_ashr_i32 s0, s2, 31
	s_lshr_b32 s0, s0, 28
	s_add_i32 s0, s2, s0
	s_ashr_i32 s18, s0, 4
	s_and_b32 s0, s0, -16
	s_sub_i32 s3, s2, s0
	s_sub_i32 s22, 31, s3
	s_mul_i32 s1, s18, 0x180000
	v_readlane_b32 s12, v253, 19
	s_mul_hi_i32 s0, s18, 0x180000
	v_readlane_b32 s13, v253, 20
	s_add_u32 s14, s12, s1
	s_addc_u32 s15, s13, s0
	v_readlane_b32 s12, v253, 15
	v_mov_b32_e32 v22, v0
	v_mov_b32_e32 v18, v224
	v_readlane_b32 s25, v251, 36
	s_cmp_gt_u32 s25, 3
	s_cbranch_scc1 .Lprio_skip_a
	s_setprio 1
